# grid barrier: acquire-side buffer_inv issued at arrival (overlaps the wait) instead of after release
# speedup vs baseline: 1.0050x; 1.0050x over previous
; __device__ __forceinline__ unsigned xb_ld(unsigned* p)              { return __hip_atomic_load(p, __ATOMIC_RELAXED, __HIP_MEMORY_SCOPE_AGENT); }
; __device__ __forceinline__ unsigned xb_add(unsigned* p, unsigned v) { return __hip_atomic_fetch_add(p, v, __ATOMIC_RELAXED, __HIP_MEMORY_SCOPE_AGENT); }
; #define XB_SPIN(cond, bar) do { unsigned _sp = 0; while (cond) { __builtin_amdgcn_s_sleep(1); \
;     if ((++_sp & 255u) == 0u) { if (xb_ld(&(bar)[XB_TMO])) break; if (_sp > XB_SPIN_CAP) { atomicAdd(&(bar)[XB_TMO], 1u); break; } } } } while (0)
; __device__ __forceinline__ void xcd_barrier(const XcdBarrier& b) {
;     ...
;     if (threadIdx.x == 0) {
;         unsigned* bar = b.bar;
;         __builtin_amdgcn_s_waitcnt(0);
;         unsigned nloc = b.st[0], nx = b.st[1];
;         if (nloc == 0u) { xcd_barrier_complete(bar, b.x, nloc, nx); b.st[0] = nloc; b.st[1] = nx; }
;         const unsigned old = xb_add(&bar[XB_XSUB(b.x)], 1u);
;         const unsigned gen = old / nloc;
;         if (old + 1u == (gen + 1u) * nloc) {
;             __builtin_amdgcn_fence(__ATOMIC_RELEASE, "agent");
;             asm volatile("s_waitcnt vmcnt(0)" ::: "memory");
;             const unsigned og = xb_add(&bar[XB_TOP], 1u);
;             const unsigned tg = og / nx;
;             if (og + 1u == (tg + 1u) * nx) xb_add(&bar[XB_TOPGEN], 1u);
;             else XB_SPIN(xb_ld(&bar[XB_TOPGEN]) == tg, bar);
;             __builtin_amdgcn_fence(__ATOMIC_ACQUIRE, "agent");
;             xb_add(&bar[XB_XGEN(b.x)], 1u);
;             asm volatile("s_waitcnt vmcnt(0)" ::: "memory");
;         } else {
;             XB_SPIN(xb_ld(&bar[XB_XGEN(b.x)]) == gen, bar);
.LBB0_42:
	s_lshl_b32 s22, s33, 6
	s_add_i32 s4, s22, 0x500
	s_mov_b32 s5, 0
	s_lshl_b64 s[0:1], s[4:5], 2
	s_add_u32 s0, s38, s0
	s_addc_u32 s1, s39, s1
	v_mov_b32_e32 v1, 1
	v_mov_b64_e32 v[6:7], s[0:1]
	flat_atomic_add v1, v[6:7], v1 sc0
	v_cvt_f32_u32_e32 v3, v4
	v_sub_u32_e32 v5, 0, v4
	v_rcp_iflag_f32_e32 v3, v3
	s_nop 0
	v_mul_f32_e32 v3, 0x4f7ffffe, v3
	v_cvt_u32_f32_e32 v3, v3
	v_mul_lo_u32 v5, v5, v3
	v_mul_hi_u32 v5, v3, v5
	v_add_u32_e32 v3, v3, v5
	s_waitcnt vmcnt(0) lgkmcnt(0)
	buffer_inv sc1
	v_mul_hi_u32 v3, v1, v3
	v_mul_lo_u32 v5, v3, v4
	v_add_u32_e32 v6, 1, v1
	v_sub_u32_e32 v1, v1, v5
	v_add_u32_e32 v7, 1, v3
	v_cmp_ge_u32_e32 vcc, v1, v4
	v_sub_u32_e32 v5, v1, v4
	s_nop 0
	v_cndmask_b32_e32 v3, v3, v7, vcc
	v_cndmask_b32_e32 v1, v1, v5, vcc
	v_add_u32_e32 v5, 1, v3
	v_cmp_ge_u32_e32 vcc, v1, v4
	s_nop 1
	v_cndmask_b32_e32 v1, v3, v5, vcc
	v_mad_u64_u32 v[4:5], s[0:1], v4, v1, v[4:5]
	v_cmp_ne_u32_e32 vcc, v6, v4
	s_and_saveexec_b64 s[0:1], vcc
	s_xor_b64 s[0:1], exec, s[0:1]
	s_cbranch_execz .LBB0_55
	s_add_i32 s4, s22, 0x900
	s_lshl_b64 s[4:5], s[4:5], 2
	s_add_u32 s6, s38, s4
	s_addc_u32 s7, s39, s5
	s_add_u32 s6, s38, 0x3500
	s_addc_u32 s7, s39, 0
	v_mov_b64_e32 v[2:3], s[6:7]
	flat_load_dword v2, v[2:3] sc1
	s_waitcnt vmcnt(0) lgkmcnt(0)
	v_cmp_eq_u32_e32 vcc, v2, v1
	s_and_saveexec_b64 s[4:5], vcc
	s_cbranch_execz .LBB0_54
	s_mov_b32 s23, 1
	s_mov_b64 s[8:9], 0
	s_branch .LBB0_46

; __device__ __forceinline__ unsigned xb_ld(unsigned* p)              { return __hip_atomic_load(p, __ATOMIC_RELAXED, __HIP_MEMORY_SCOPE_AGENT); }
; #define XB_SPIN(cond, bar) do { unsigned _sp = 0; while (cond) { __builtin_amdgcn_s_sleep(1); \
;     if ((++_sp & 255u) == 0u) { if (xb_ld(&(bar)[XB_TMO])) break; if (_sp > XB_SPIN_CAP) { atomicAdd(&(bar)[XB_TMO], 1u); break; } } } } while (0)
; __device__ __forceinline__ void xcd_barrier(const XcdBarrier& b) {
;     ...
;             XB_SPIN(xb_ld(&bar[XB_XGEN(b.x)]) == gen, bar);
;             __builtin_amdgcn_fence(__ATOMIC_ACQUIRE, "agent");
;             asm volatile("s_waitcnt vmcnt(0)" ::: "memory");
.LBB0_54:
	s_or_b64 exec, exec, s[4:5]
	s_waitcnt vmcnt(0) lgkmcnt(0)
	s_waitcnt vmcnt(0)

; __device__ __forceinline__ unsigned xb_add(unsigned* p, unsigned v) { return __hip_atomic_fetch_add(p, v, __ATOMIC_RELAXED, __HIP_MEMORY_SCOPE_AGENT); }
; __device__ __forceinline__ void xcd_barrier(const XcdBarrier& b) {
;     ...
;             __builtin_amdgcn_fence(__ATOMIC_ACQUIRE, "agent");
;             xb_add(&bar[XB_XGEN(b.x)], 1u);
;             asm volatile("s_waitcnt vmcnt(0)" ::: "memory");
.LBB0_70:
	s_or_b64 exec, exec, s[0:1]
	s_add_i32 s0, s22, 0x900
	s_mov_b32 s1, 0
	s_lshl_b64 s[0:1], s[0:1], 2
	s_add_u32 s0, s38, s0
	s_addc_u32 s1, s39, s1
	v_mov_b32_e32 v1, 1
	v_mov_b64_e32 v[2:3], s[0:1]
	s_waitcnt vmcnt(0) lgkmcnt(0)
	flat_atomic_add v[2:3], v1
	s_waitcnt vmcnt(0)

; __device__ __forceinline__ unsigned xb_ld(unsigned* p)              { return __hip_atomic_load(p, __ATOMIC_RELAXED, __HIP_MEMORY_SCOPE_AGENT); }
; __device__ __forceinline__ unsigned xb_add(unsigned* p, unsigned v) { return __hip_atomic_fetch_add(p, v, __ATOMIC_RELAXED, __HIP_MEMORY_SCOPE_AGENT); }
; #define XB_SPIN(cond, bar) do { unsigned _sp = 0; while (cond) { __builtin_amdgcn_s_sleep(1); \
;     if ((++_sp & 255u) == 0u) { if (xb_ld(&(bar)[XB_TMO])) break; if (_sp > XB_SPIN_CAP) { atomicAdd(&(bar)[XB_TMO], 1u); break; } } } } while (0)
; __device__ __forceinline__ void xcd_barrier(const XcdBarrier& b) {
;     ...
;     if (threadIdx.x == 0) {
;         unsigned* bar = b.bar;
;         __builtin_amdgcn_s_waitcnt(0);
;         unsigned nloc = b.st[0], nx = b.st[1];
;         if (nloc == 0u) { xcd_barrier_complete(bar, b.x, nloc, nx); b.st[0] = nloc; b.st[1] = nx; }
;         const unsigned old = xb_add(&bar[XB_XSUB(b.x)], 1u);
;         const unsigned gen = old / nloc;
;         if (old + 1u == (gen + 1u) * nloc) {
;             __builtin_amdgcn_fence(__ATOMIC_RELEASE, "agent");
;             asm volatile("s_waitcnt vmcnt(0)" ::: "memory");
;             const unsigned og = xb_add(&bar[XB_TOP], 1u);
;             const unsigned tg = og / nx;
;             if (og + 1u == (tg + 1u) * nx) xb_add(&bar[XB_TOPGEN], 1u);
;             else XB_SPIN(xb_ld(&bar[XB_TOPGEN]) == tg, bar);
;             __builtin_amdgcn_fence(__ATOMIC_ACQUIRE, "agent");
;             xb_add(&bar[XB_XGEN(b.x)], 1u);
;             asm volatile("s_waitcnt vmcnt(0)" ::: "memory");
;         } else {
;             XB_SPIN(xb_ld(&bar[XB_XGEN(b.x)]) == gen, bar);
.LBB0_177:
	s_lshl_b32 s22, s36, 6
	s_add_i32 s4, s22, 0x500
	s_mov_b32 s5, 0
	s_lshl_b64 s[0:1], s[4:5], 2
	s_add_u32 s0, s34, s0
	s_addc_u32 s1, s35, s1
	v_mov_b32_e32 v1, 1
	v_mov_b64_e32 v[6:7], s[0:1]
	flat_atomic_add v1, v[6:7], v1 sc0
	v_cvt_f32_u32_e32 v3, v4
	v_sub_u32_e32 v5, 0, v4
	v_rcp_iflag_f32_e32 v3, v3
	s_nop 0
	v_mul_f32_e32 v3, 0x4f7ffffe, v3
	v_cvt_u32_f32_e32 v3, v3
	v_mul_lo_u32 v5, v5, v3
	v_mul_hi_u32 v5, v3, v5
	v_add_u32_e32 v3, v3, v5
	s_waitcnt vmcnt(0) lgkmcnt(0)
	buffer_inv sc1
	v_mul_hi_u32 v3, v1, v3
	v_mul_lo_u32 v5, v3, v4
	v_add_u32_e32 v6, 1, v1
	v_sub_u32_e32 v1, v1, v5
	v_add_u32_e32 v7, 1, v3
	v_cmp_ge_u32_e32 vcc, v1, v4
	v_sub_u32_e32 v5, v1, v4
	s_nop 0
	v_cndmask_b32_e32 v3, v3, v7, vcc
	v_cndmask_b32_e32 v1, v1, v5, vcc
	v_add_u32_e32 v5, 1, v3
	v_cmp_ge_u32_e32 vcc, v1, v4
	s_nop 1
	v_cndmask_b32_e32 v1, v3, v5, vcc
	v_mad_u64_u32 v[4:5], s[0:1], v4, v1, v[4:5]
	v_cmp_ne_u32_e32 vcc, v6, v4
	s_and_saveexec_b64 s[0:1], vcc
	s_xor_b64 s[0:1], exec, s[0:1]
	s_cbranch_execz .LBB0_190
	s_add_i32 s4, s22, 0x900
	s_lshl_b64 s[4:5], s[4:5], 2
	s_add_u32 s6, s34, s4
	s_addc_u32 s7, s35, s5
	s_add_u32 s6, s34, 0x3500
	s_addc_u32 s7, s35, 0
	v_mov_b64_e32 v[2:3], s[6:7]
	flat_load_dword v2, v[2:3] sc1
	s_waitcnt vmcnt(0) lgkmcnt(0)
	v_cmp_eq_u32_e32 vcc, v2, v1
	s_and_saveexec_b64 s[4:5], vcc
	s_cbranch_execz .LBB0_189
	s_mov_b32 s23, 1
	s_mov_b64 s[8:9], 0
	s_branch .LBB0_181

; __device__ __forceinline__ unsigned xb_add(unsigned* p, unsigned v) { return __hip_atomic_fetch_add(p, v, __ATOMIC_RELAXED, __HIP_MEMORY_SCOPE_AGENT); }
; __device__ __forceinline__ void xcd_barrier(const XcdBarrier& b) {
;     ...
;             __builtin_amdgcn_fence(__ATOMIC_ACQUIRE, "agent");
;             xb_add(&bar[XB_XGEN(b.x)], 1u);
;             asm volatile("s_waitcnt vmcnt(0)" ::: "memory");
.LBB0_205:
	s_or_b64 exec, exec, s[0:1]
	s_add_i32 s0, s22, 0x900
	s_mov_b32 s1, 0
	s_lshl_b64 s[0:1], s[0:1], 2
	s_add_u32 s0, s34, s0
	s_addc_u32 s1, s35, s1
	v_mov_b32_e32 v1, 1
	v_mov_b64_e32 v[2:3], s[0:1]
	s_waitcnt vmcnt(0) lgkmcnt(0)
	flat_atomic_add v[2:3], v1
	s_waitcnt vmcnt(0)

; __device__ __forceinline__ unsigned xb_ld(unsigned* p)              { return __hip_atomic_load(p, __ATOMIC_RELAXED, __HIP_MEMORY_SCOPE_AGENT); }
; __device__ __forceinline__ unsigned xb_add(unsigned* p, unsigned v) { return __hip_atomic_fetch_add(p, v, __ATOMIC_RELAXED, __HIP_MEMORY_SCOPE_AGENT); }
; #define XB_SPIN(cond, bar) do { unsigned _sp = 0; while (cond) { __builtin_amdgcn_s_sleep(1); \
;     if ((++_sp & 255u) == 0u) { if (xb_ld(&(bar)[XB_TMO])) break; if (_sp > XB_SPIN_CAP) { atomicAdd(&(bar)[XB_TMO], 1u); break; } } } } while (0)
; __device__ __forceinline__ void xcd_barrier_host(const XcdBarrier& b, Frame& F, unsigned epoch) {
;     ...
;         __builtin_amdgcn_s_waitcnt(0);
;         unsigned nloc = b.st[0], nx = b.st[1];
;         if (nloc == 0u) { xcd_barrier_complete(bar, b.x, nloc, nx); b.st[0] = nloc; b.st[1] = nx; }
;         const unsigned old = xb_add(&bar[XB_XSUB(b.x)], 1u);
;         const unsigned gen = old / nloc;
;         if (old + 1u == (gen + 1u) * nloc) {
;             __builtin_amdgcn_fence(__ATOMIC_RELEASE, "agent");
;             asm volatile("s_waitcnt vmcnt(0)" ::: "memory");
;             const unsigned og = xb_add(&bar[XB_TOP], 1u);
;             const unsigned tg = og / nx;
;             if (og + 1u == (tg + 1u) * nx) xb_add(&bar[XB_TOPGEN], 1u);
;             else XB_SPIN(xb_ld(&bar[XB_TOPGEN]) == tg, bar);
;             __builtin_amdgcn_fence(__ATOMIC_ACQUIRE, "agent");
;             xb_add(&bar[XB_XGEN(b.x)], 1u);
;             asm volatile("s_waitcnt vmcnt(0)" ::: "memory");
;         } else {
;             XB_SPIN(xb_ld(&bar[XB_XGEN(b.x)]) == gen, bar);
.LBB0_247:
	s_lshl_b32 s24, s36, 6
	s_add_i32 s4, s24, 0x500
	s_mov_b32 s5, 0
	s_lshl_b64 s[0:1], s[4:5], 2
	s_add_u32 s0, s34, s0
	s_addc_u32 s1, s35, s1
	v_mov_b32_e32 v1, 1
	v_mov_b64_e32 v[6:7], s[0:1]
	flat_atomic_add v1, v[6:7], v1 sc0
	v_cvt_f32_u32_e32 v3, v4
	v_sub_u32_e32 v5, 0, v4
	v_rcp_iflag_f32_e32 v3, v3
	s_nop 0
	v_mul_f32_e32 v3, 0x4f7ffffe, v3
	v_cvt_u32_f32_e32 v3, v3
	v_mul_lo_u32 v5, v5, v3
	v_mul_hi_u32 v5, v3, v5
	v_add_u32_e32 v3, v3, v5
	s_waitcnt vmcnt(0) lgkmcnt(0)
	buffer_inv sc1
	v_mul_hi_u32 v3, v1, v3
	v_mul_lo_u32 v5, v3, v4
	v_add_u32_e32 v6, 1, v1
	v_sub_u32_e32 v1, v1, v5
	v_add_u32_e32 v7, 1, v3
	v_cmp_ge_u32_e32 vcc, v1, v4
	v_sub_u32_e32 v5, v1, v4
	s_nop 0
	v_cndmask_b32_e32 v3, v3, v7, vcc
	v_cndmask_b32_e32 v1, v1, v5, vcc
	v_add_u32_e32 v5, 1, v3
	v_cmp_ge_u32_e32 vcc, v1, v4
	s_nop 1
	v_cndmask_b32_e32 v1, v3, v5, vcc
	v_mad_u64_u32 v[4:5], s[0:1], v4, v1, v[4:5]
	v_cmp_ne_u32_e32 vcc, v6, v4
	s_and_saveexec_b64 s[0:1], vcc
	s_xor_b64 s[0:1], exec, s[0:1]
	s_cbranch_execz .LBB0_260
	s_add_i32 s4, s24, 0x900
	s_lshl_b64 s[4:5], s[4:5], 2
	s_add_u32 s6, s34, s4
	s_addc_u32 s7, s35, s5
	s_add_u32 s6, s34, 0x3500
	s_addc_u32 s7, s35, 0
	v_mov_b64_e32 v[2:3], s[6:7]
	flat_load_dword v2, v[2:3] sc1
	s_waitcnt vmcnt(0) lgkmcnt(0)
	v_cmp_eq_u32_e32 vcc, v2, v1
	s_and_saveexec_b64 s[4:5], vcc
	s_cbranch_execz .LBB0_259
	s_mov_b32 s22, 1
	s_mov_b64 s[8:9], 0
	s_branch .LBB0_251

; __device__ __forceinline__ unsigned xb_add(unsigned* p, unsigned v) { return __hip_atomic_fetch_add(p, v, __ATOMIC_RELAXED, __HIP_MEMORY_SCOPE_AGENT); }
; __device__ __forceinline__ void xcd_barrier_host(const XcdBarrier& b, Frame& F, unsigned epoch) {
;     ...
;             __builtin_amdgcn_fence(__ATOMIC_ACQUIRE, "agent");
;             xb_add(&bar[XB_XGEN(b.x)], 1u);
;             asm volatile("s_waitcnt vmcnt(0)" ::: "memory");
.LBB0_275:
	s_or_b64 exec, exec, s[4:5]
	s_add_i32 s4, s24, 0x900
	s_mov_b32 s5, 0
	s_lshl_b64 s[4:5], s[4:5], 2
	s_add_u32 s4, s34, s4
	s_addc_u32 s5, s35, s5
	v_mov_b32_e32 v1, 1
	v_mov_b64_e32 v[2:3], s[4:5]
	s_waitcnt vmcnt(0) lgkmcnt(0)
	flat_atomic_add v[2:3], v1
	s_waitcnt vmcnt(0)

; __device__ __forceinline__ unsigned xb_add(unsigned* p, unsigned v) { return __hip_atomic_fetch_add(p, v, __ATOMIC_RELAXED, __HIP_MEMORY_SCOPE_AGENT); }
; __device__ __forceinline__ void xcd_barrier_host(const XcdBarrier& b, Frame& F, unsigned epoch) {
;     ...
;             __builtin_amdgcn_fence(__ATOMIC_ACQUIRE, "agent");
;             xb_add(&bar[XB_XGEN(b.x)], 1u);
;             asm volatile("s_waitcnt vmcnt(0)" ::: "memory");
.LBB0_281:
	s_or_b64 exec, exec, s[4:5]
	s_add_i32 s94, s24, 0x900
	s_lshl_b64 s[4:5], s[94:95], 2
	s_add_u32 s4, s34, s4
	s_addc_u32 s5, s35, s5
	v_mov_b64_e32 v[2:3], s[4:5]
	s_waitcnt vmcnt(0) lgkmcnt(0)
	flat_atomic_add v[2:3], v224
	s_waitcnt vmcnt(0)

; __device__ __forceinline__ unsigned xb_ld(unsigned* p)              { return __hip_atomic_load(p, __ATOMIC_RELAXED, __HIP_MEMORY_SCOPE_AGENT); }
; __device__ __forceinline__ unsigned xb_add(unsigned* p, unsigned v) { return __hip_atomic_fetch_add(p, v, __ATOMIC_RELAXED, __HIP_MEMORY_SCOPE_AGENT); }
; #define XB_SPIN(cond, bar) do { unsigned _sp = 0; while (cond) { __builtin_amdgcn_s_sleep(1); \
;     if ((++_sp & 255u) == 0u) { if (xb_ld(&(bar)[XB_TMO])) break; if (_sp > XB_SPIN_CAP) { atomicAdd(&(bar)[XB_TMO], 1u); break; } } } } while (0)
; __device__ __forceinline__ void xcd_barrier(const XcdBarrier& b) {
;     ...
;     if (threadIdx.x == 0) {
;         unsigned* bar = b.bar;
;         __builtin_amdgcn_s_waitcnt(0);
;         unsigned nloc = b.st[0], nx = b.st[1];
;         if (nloc == 0u) { xcd_barrier_complete(bar, b.x, nloc, nx); b.st[0] = nloc; b.st[1] = nx; }
;         const unsigned old = xb_add(&bar[XB_XSUB(b.x)], 1u);
;         const unsigned gen = old / nloc;
;         if (old + 1u == (gen + 1u) * nloc) {
;             __builtin_amdgcn_fence(__ATOMIC_RELEASE, "agent");
;             asm volatile("s_waitcnt vmcnt(0)" ::: "memory");
;             const unsigned og = xb_add(&bar[XB_TOP], 1u);
;             const unsigned tg = og / nx;
;             if (og + 1u == (tg + 1u) * nx) xb_add(&bar[XB_TOPGEN], 1u);
;             else XB_SPIN(xb_ld(&bar[XB_TOPGEN]) == tg, bar);
;             __builtin_amdgcn_fence(__ATOMIC_ACQUIRE, "agent");
;             xb_add(&bar[XB_XGEN(b.x)], 1u);
;             asm volatile("s_waitcnt vmcnt(0)" ::: "memory");
;         } else {
;             XB_SPIN(xb_ld(&bar[XB_XGEN(b.x)]) == gen, bar);
.LBB0_346:
	s_lshl_b32 s22, s39, 6
	s_add_i32 s94, s22, 0x500
	s_lshl_b64 s[0:1], s[94:95], 2
	s_add_u32 s0, s36, s0
	s_addc_u32 s1, s37, s1
	v_mov_b64_e32 v[6:7], s[0:1]
	flat_atomic_add v3, v[6:7], v224 sc0
	v_cvt_f32_u32_e32 v1, v4
	v_sub_u32_e32 v5, 0, v4
	v_rcp_iflag_f32_e32 v1, v1
	s_nop 0
	v_mul_f32_e32 v1, 0x4f7ffffe, v1
	v_cvt_u32_f32_e32 v1, v1
	v_mul_lo_u32 v5, v5, v1
	v_mul_hi_u32 v5, v1, v5
	v_add_u32_e32 v1, v1, v5
	s_waitcnt vmcnt(0) lgkmcnt(0)
	buffer_inv sc1
	v_mul_hi_u32 v1, v3, v1
	v_mul_lo_u32 v5, v1, v4
	v_sub_u32_e32 v5, v3, v5
	v_cmp_ge_u32_e32 vcc, v5, v4
	v_add_u32_e32 v6, 1, v1
	v_add_u32_e32 v3, 1, v3
	v_cndmask_b32_e32 v1, v1, v6, vcc
	v_sub_u32_e32 v6, v5, v4
	v_cndmask_b32_e32 v5, v5, v6, vcc
	v_cmp_ge_u32_e32 vcc, v5, v4
	v_add_u32_e32 v5, 1, v1
	s_nop 0
	v_cndmask_b32_e32 v1, v1, v5, vcc
	v_mad_u64_u32 v[4:5], s[0:1], v4, v1, v[4:5]
	v_cmp_ne_u32_e32 vcc, v3, v4
	s_and_saveexec_b64 s[0:1], vcc
	s_xor_b64 s[0:1], exec, s[0:1]
	s_cbranch_execz .LBB0_359
	s_add_i32 s94, s22, 0x900
	s_lshl_b64 s[4:5], s[94:95], 2
	s_add_u32 s6, s36, s4
	s_addc_u32 s7, s37, s5
	s_add_u32 s6, s36, 0x3500
	s_addc_u32 s7, s37, 0
	v_mov_b64_e32 v[2:3], s[6:7]
	flat_load_dword v2, v[2:3] sc1
	s_waitcnt vmcnt(0) lgkmcnt(0)
	v_cmp_eq_u32_e32 vcc, v2, v1
	s_and_saveexec_b64 s[4:5], vcc
	s_cbranch_execz .LBB0_358
	s_mov_b32 s23, 1
	s_mov_b64 s[8:9], 0
	s_branch .LBB0_350

; __device__ __forceinline__ unsigned xb_add(unsigned* p, unsigned v) { return __hip_atomic_fetch_add(p, v, __ATOMIC_RELAXED, __HIP_MEMORY_SCOPE_AGENT); }
; __device__ __forceinline__ void xcd_barrier(const XcdBarrier& b) {
;     ...
;             __builtin_amdgcn_fence(__ATOMIC_ACQUIRE, "agent");
;             xb_add(&bar[XB_XGEN(b.x)], 1u);
;             asm volatile("s_waitcnt vmcnt(0)" ::: "memory");
.LBB0_374:
	s_or_b64 exec, exec, s[0:1]
	s_add_i32 s94, s22, 0x900
	s_lshl_b64 s[0:1], s[94:95], 2
	s_add_u32 s0, s36, s0
	s_addc_u32 s1, s37, s1
	v_mov_b64_e32 v[2:3], s[0:1]
	s_waitcnt vmcnt(0) lgkmcnt(0)
	flat_atomic_add v[2:3], v224
	s_waitcnt vmcnt(0)

; __device__ __forceinline__ unsigned xb_ld(unsigned* p)              { return __hip_atomic_load(p, __ATOMIC_RELAXED, __HIP_MEMORY_SCOPE_AGENT); }
; __device__ __forceinline__ unsigned xb_add(unsigned* p, unsigned v) { return __hip_atomic_fetch_add(p, v, __ATOMIC_RELAXED, __HIP_MEMORY_SCOPE_AGENT); }
; #define XB_SPIN(cond, bar) do { unsigned _sp = 0; while (cond) { __builtin_amdgcn_s_sleep(1); \
;     if ((++_sp & 255u) == 0u) { if (xb_ld(&(bar)[XB_TMO])) break; if (_sp > XB_SPIN_CAP) { atomicAdd(&(bar)[XB_TMO], 1u); break; } } } } while (0)
; __device__ __forceinline__ void xcd_barrier_host(const XcdBarrier& b, Frame& F, unsigned epoch) {
;     ...
;         __builtin_amdgcn_s_waitcnt(0);
;         unsigned nloc = b.st[0], nx = b.st[1];
;         if (nloc == 0u) { xcd_barrier_complete(bar, b.x, nloc, nx); b.st[0] = nloc; b.st[1] = nx; }
;         const unsigned old = xb_add(&bar[XB_XSUB(b.x)], 1u);
;         const unsigned gen = old / nloc;
;         if (old + 1u == (gen + 1u) * nloc) {
;             __builtin_amdgcn_fence(__ATOMIC_RELEASE, "agent");
;             asm volatile("s_waitcnt vmcnt(0)" ::: "memory");
;             const unsigned og = xb_add(&bar[XB_TOP], 1u);
;             const unsigned tg = og / nx;
;             if (og + 1u == (tg + 1u) * nx) xb_add(&bar[XB_TOPGEN], 1u);
;             else XB_SPIN(xb_ld(&bar[XB_TOPGEN]) == tg, bar);
;             __builtin_amdgcn_fence(__ATOMIC_ACQUIRE, "agent");
;             xb_add(&bar[XB_XGEN(b.x)], 1u);
;             asm volatile("s_waitcnt vmcnt(0)" ::: "memory");
;         } else {
;             XB_SPIN(xb_ld(&bar[XB_XGEN(b.x)]) == gen, bar);
.LBB0_416:
	s_lshl_b32 s24, s39, 6
	s_add_i32 s94, s24, 0x500
	s_lshl_b64 s[0:1], s[94:95], 2
	s_add_u32 s0, s36, s0
	s_addc_u32 s1, s37, s1
	v_mov_b64_e32 v[6:7], s[0:1]
	flat_atomic_add v3, v[6:7], v224 sc0
	v_cvt_f32_u32_e32 v1, v4
	v_sub_u32_e32 v5, 0, v4
	v_rcp_iflag_f32_e32 v1, v1
	s_nop 0
	v_mul_f32_e32 v1, 0x4f7ffffe, v1
	v_cvt_u32_f32_e32 v1, v1
	v_mul_lo_u32 v5, v5, v1
	v_mul_hi_u32 v5, v1, v5
	v_add_u32_e32 v1, v1, v5
	s_waitcnt vmcnt(0) lgkmcnt(0)
	buffer_inv sc1
	v_mul_hi_u32 v1, v3, v1
	v_mul_lo_u32 v5, v1, v4
	v_sub_u32_e32 v5, v3, v5
	v_cmp_ge_u32_e32 vcc, v5, v4
	v_add_u32_e32 v6, 1, v1
	v_add_u32_e32 v3, 1, v3
	v_cndmask_b32_e32 v1, v1, v6, vcc
	v_sub_u32_e32 v6, v5, v4
	v_cndmask_b32_e32 v5, v5, v6, vcc
	v_cmp_ge_u32_e32 vcc, v5, v4
	v_add_u32_e32 v5, 1, v1
	s_nop 0
	v_cndmask_b32_e32 v1, v1, v5, vcc
	v_mad_u64_u32 v[4:5], s[0:1], v4, v1, v[4:5]
	v_cmp_ne_u32_e32 vcc, v3, v4
	s_and_saveexec_b64 s[0:1], vcc
	s_xor_b64 s[0:1], exec, s[0:1]
	s_cbranch_execz .LBB0_429
	s_add_i32 s94, s24, 0x900
	s_lshl_b64 s[4:5], s[94:95], 2
	s_add_u32 s6, s36, s4
	s_addc_u32 s7, s37, s5
	s_add_u32 s6, s36, 0x3500
	s_addc_u32 s7, s37, 0
	v_mov_b64_e32 v[2:3], s[6:7]
	flat_load_dword v2, v[2:3] sc1
	s_waitcnt vmcnt(0) lgkmcnt(0)
	v_cmp_eq_u32_e32 vcc, v2, v1
	s_and_saveexec_b64 s[4:5], vcc
	s_cbranch_execz .LBB0_428
	s_mov_b32 s22, 1
	s_mov_b64 s[8:9], 0
	s_branch .LBB0_420

; __device__ __forceinline__ unsigned xb_add(unsigned* p, unsigned v) { return __hip_atomic_fetch_add(p, v, __ATOMIC_RELAXED, __HIP_MEMORY_SCOPE_AGENT); }
; __device__ __forceinline__ void xcd_barrier_host(const XcdBarrier& b, Frame& F, unsigned epoch) {
;     ...
;             __builtin_amdgcn_fence(__ATOMIC_ACQUIRE, "agent");
;             xb_add(&bar[XB_XGEN(b.x)], 1u);
;             asm volatile("s_waitcnt vmcnt(0)" ::: "memory");
.LBB0_444:
	s_or_b64 exec, exec, s[4:5]
	s_add_i32 s94, s24, 0x900
	s_lshl_b64 s[4:5], s[94:95], 2
	s_add_u32 s4, s36, s4
	s_addc_u32 s5, s37, s5
	v_mov_b64_e32 v[2:3], s[4:5]
	s_waitcnt vmcnt(0) lgkmcnt(0)
	flat_atomic_add v[2:3], v224
	s_waitcnt vmcnt(0)

; __device__ __forceinline__ unsigned xb_ld(unsigned* p)              { return __hip_atomic_load(p, __ATOMIC_RELAXED, __HIP_MEMORY_SCOPE_AGENT); }
; __device__ __forceinline__ unsigned xb_add(unsigned* p, unsigned v) { return __hip_atomic_fetch_add(p, v, __ATOMIC_RELAXED, __HIP_MEMORY_SCOPE_AGENT); }
; #define XB_SPIN(cond, bar) do { unsigned _sp = 0; while (cond) { __builtin_amdgcn_s_sleep(1); \
;     if ((++_sp & 255u) == 0u) { if (xb_ld(&(bar)[XB_TMO])) break; if (_sp > XB_SPIN_CAP) { atomicAdd(&(bar)[XB_TMO], 1u); break; } } } } while (0)
; __device__ __forceinline__ void xcd_barrier(const XcdBarrier& b) {
;     ...
;     if (threadIdx.x == 0) {
;         unsigned* bar = b.bar;
;         __builtin_amdgcn_s_waitcnt(0);
;         unsigned nloc = b.st[0], nx = b.st[1];
;         if (nloc == 0u) { xcd_barrier_complete(bar, b.x, nloc, nx); b.st[0] = nloc; b.st[1] = nx; }
;         const unsigned old = xb_add(&bar[XB_XSUB(b.x)], 1u);
;         const unsigned gen = old / nloc;
;         if (old + 1u == (gen + 1u) * nloc) {
;             __builtin_amdgcn_fence(__ATOMIC_RELEASE, "agent");
;             asm volatile("s_waitcnt vmcnt(0)" ::: "memory");
;             const unsigned og = xb_add(&bar[XB_TOP], 1u);
;             const unsigned tg = og / nx;
;             if (og + 1u == (tg + 1u) * nx) xb_add(&bar[XB_TOPGEN], 1u);
;             else XB_SPIN(xb_ld(&bar[XB_TOPGEN]) == tg, bar);
;             __builtin_amdgcn_fence(__ATOMIC_ACQUIRE, "agent");
;             xb_add(&bar[XB_XGEN(b.x)], 1u);
;             asm volatile("s_waitcnt vmcnt(0)" ::: "memory");
;         } else {
;             XB_SPIN(xb_ld(&bar[XB_XGEN(b.x)]) == gen, bar);
.LBB0_2013:
	s_lshl_b32 s22, s37, 6
	s_add_i32 s94, s22, 0x500
	s_lshl_b64 s[0:1], s[94:95], 2
	s_add_u32 s0, s34, s0
	s_addc_u32 s1, s35, s1
	v_mov_b64_e32 v[6:7], s[0:1]
	flat_atomic_add v3, v[6:7], v224 sc0
	v_cvt_f32_u32_e32 v1, v4
	v_sub_u32_e32 v5, 0, v4
	v_rcp_iflag_f32_e32 v1, v1
	s_nop 0
	v_mul_f32_e32 v1, 0x4f7ffffe, v1
	v_cvt_u32_f32_e32 v1, v1
	v_mul_lo_u32 v5, v5, v1
	v_mul_hi_u32 v5, v1, v5
	v_add_u32_e32 v1, v1, v5
	s_waitcnt vmcnt(0) lgkmcnt(0)
	buffer_inv sc1
	v_mul_hi_u32 v1, v3, v1
	v_mul_lo_u32 v5, v1, v4
	v_sub_u32_e32 v5, v3, v5
	v_cmp_ge_u32_e32 vcc, v5, v4
	v_add_u32_e32 v6, 1, v1
	v_add_u32_e32 v3, 1, v3
	v_cndmask_b32_e32 v1, v1, v6, vcc
	v_sub_u32_e32 v6, v5, v4
	v_cndmask_b32_e32 v5, v5, v6, vcc
	v_cmp_ge_u32_e32 vcc, v5, v4
	v_add_u32_e32 v5, 1, v1
	s_nop 0
	v_cndmask_b32_e32 v1, v1, v5, vcc
	v_mad_u64_u32 v[4:5], s[0:1], v4, v1, v[4:5]
	v_cmp_ne_u32_e32 vcc, v3, v4
	s_and_saveexec_b64 s[0:1], vcc
	v_readlane_b32 s30, v255, 3
	s_xor_b64 s[0:1], exec, s[0:1]
	v_readlane_b32 s31, v255, 4
	s_cbranch_execz .LBB0_2026
	s_add_i32 s94, s22, 0x900
	s_lshl_b64 s[4:5], s[94:95], 2
	s_add_u32 s6, s34, s4
	s_addc_u32 s7, s35, s5
	s_add_u32 s6, s34, 0x3500
	s_addc_u32 s7, s35, 0
	v_mov_b64_e32 v[2:3], s[6:7]
	flat_load_dword v2, v[2:3] sc1
	s_waitcnt vmcnt(0) lgkmcnt(0)
	v_cmp_eq_u32_e32 vcc, v2, v1
	s_and_saveexec_b64 s[4:5], vcc
	s_cbranch_execz .LBB0_2025
	s_mov_b32 s23, 1
	s_mov_b64 s[8:9], 0
	s_branch .LBB0_2017

; __device__ __forceinline__ unsigned xb_add(unsigned* p, unsigned v) { return __hip_atomic_fetch_add(p, v, __ATOMIC_RELAXED, __HIP_MEMORY_SCOPE_AGENT); }
; __device__ __forceinline__ void xcd_barrier(const XcdBarrier& b) {
;     ...
;             __builtin_amdgcn_fence(__ATOMIC_ACQUIRE, "agent");
;             xb_add(&bar[XB_XGEN(b.x)], 1u);
;             asm volatile("s_waitcnt vmcnt(0)" ::: "memory");
.LBB0_2041:
	s_or_b64 exec, exec, s[0:1]
	s_add_i32 s94, s22, 0x900
	s_lshl_b64 s[0:1], s[94:95], 2
	s_add_u32 s0, s34, s0
	s_addc_u32 s1, s35, s1
	v_mov_b64_e32 v[2:3], s[0:1]
	s_waitcnt vmcnt(0) lgkmcnt(0)
	flat_atomic_add v[2:3], v224
	s_waitcnt vmcnt(0)

; __device__ __forceinline__ unsigned xb_ld(unsigned* p)              { return __hip_atomic_load(p, __ATOMIC_RELAXED, __HIP_MEMORY_SCOPE_AGENT); }
; __device__ __forceinline__ unsigned xb_add(unsigned* p, unsigned v) { return __hip_atomic_fetch_add(p, v, __ATOMIC_RELAXED, __HIP_MEMORY_SCOPE_AGENT); }
; #define XB_SPIN(cond, bar) do { unsigned _sp = 0; while (cond) { __builtin_amdgcn_s_sleep(1); \
;     if ((++_sp & 255u) == 0u) { if (xb_ld(&(bar)[XB_TMO])) break; if (_sp > XB_SPIN_CAP) { atomicAdd(&(bar)[XB_TMO], 1u); break; } } } } while (0)
; __device__ __forceinline__ void xcd_barrier_host(const XcdBarrier& b, Frame& F, unsigned epoch) {
;     ...
;         __builtin_amdgcn_s_waitcnt(0);
;         unsigned nloc = b.st[0], nx = b.st[1];
;         if (nloc == 0u) { xcd_barrier_complete(bar, b.x, nloc, nx); b.st[0] = nloc; b.st[1] = nx; }
;         const unsigned old = xb_add(&bar[XB_XSUB(b.x)], 1u);
;         const unsigned gen = old / nloc;
;         if (old + 1u == (gen + 1u) * nloc) {
;             __builtin_amdgcn_fence(__ATOMIC_RELEASE, "agent");
;             asm volatile("s_waitcnt vmcnt(0)" ::: "memory");
;             const unsigned og = xb_add(&bar[XB_TOP], 1u);
;             const unsigned tg = og / nx;
;             if (og + 1u == (tg + 1u) * nx) xb_add(&bar[XB_TOPGEN], 1u);
;             else XB_SPIN(xb_ld(&bar[XB_TOPGEN]) == tg, bar);
;             __builtin_amdgcn_fence(__ATOMIC_ACQUIRE, "agent");
;             xb_add(&bar[XB_XGEN(b.x)], 1u);
;             asm volatile("s_waitcnt vmcnt(0)" ::: "memory");
;         } else {
;             XB_SPIN(xb_ld(&bar[XB_XGEN(b.x)]) == gen, bar);
.LBB0_2083:
	s_lshl_b32 s24, s37, 6
	s_add_i32 s94, s24, 0x500
	s_lshl_b64 s[0:1], s[94:95], 2
	s_add_u32 s0, s34, s0
	s_addc_u32 s1, s35, s1
	v_mov_b64_e32 v[6:7], s[0:1]
	flat_atomic_add v3, v[6:7], v224 sc0
	v_cvt_f32_u32_e32 v1, v4
	v_sub_u32_e32 v5, 0, v4
	v_rcp_iflag_f32_e32 v1, v1
	s_nop 0
	v_mul_f32_e32 v1, 0x4f7ffffe, v1
	v_cvt_u32_f32_e32 v1, v1
	v_mul_lo_u32 v5, v5, v1
	v_mul_hi_u32 v5, v1, v5
	v_add_u32_e32 v1, v1, v5
	s_waitcnt vmcnt(0) lgkmcnt(0)
	buffer_inv sc1
	v_mul_hi_u32 v1, v3, v1
	v_mul_lo_u32 v5, v1, v4
	v_sub_u32_e32 v5, v3, v5
	v_cmp_ge_u32_e32 vcc, v5, v4
	v_add_u32_e32 v6, 1, v1
	v_add_u32_e32 v3, 1, v3
	v_cndmask_b32_e32 v1, v1, v6, vcc
	v_sub_u32_e32 v6, v5, v4
	v_cndmask_b32_e32 v5, v5, v6, vcc
	v_cmp_ge_u32_e32 vcc, v5, v4
	v_add_u32_e32 v5, 1, v1
	s_nop 0
	v_cndmask_b32_e32 v1, v1, v5, vcc
	v_mad_u64_u32 v[4:5], s[0:1], v4, v1, v[4:5]
	v_cmp_ne_u32_e32 vcc, v3, v4
	s_and_saveexec_b64 s[0:1], vcc
	v_readlane_b32 s30, v255, 3
	s_xor_b64 s[0:1], exec, s[0:1]
	v_readlane_b32 s31, v255, 4
	s_cbranch_execz .LBB0_2096
	s_add_i32 s94, s24, 0x900
	s_lshl_b64 s[4:5], s[94:95], 2
	s_add_u32 s6, s34, s4
	s_addc_u32 s7, s35, s5
	s_add_u32 s6, s34, 0x3500
	s_addc_u32 s7, s35, 0
	v_mov_b64_e32 v[2:3], s[6:7]
	flat_load_dword v2, v[2:3] sc1
	s_waitcnt vmcnt(0) lgkmcnt(0)
	v_cmp_eq_u32_e32 vcc, v2, v1
	s_and_saveexec_b64 s[4:5], vcc
	s_cbranch_execz .LBB0_2095
	s_mov_b32 s22, 1
	s_mov_b64 s[8:9], 0
	s_branch .LBB0_2087
